# LRU loop: top-of-unit vmcnt(0) (waited only for the previous unit's stores) relaxed to a counted vmcnt(15); full waits kept on the weight-reload path and in the preheader
# baseline (speedup 1.0000x reference)
; #define LAS __attribute__((address_space(3)))
; __device__ __forceinline__ int phase_tid() { int t = (int)threadIdx.x; asm volatile("" : "+v"(t)); return t; }
; __device__ __forceinline__ int phase_wid(int tid) { return __builtin_amdgcn_readfirstlane(tid >> 6); }
; template <int MODE> ...
;     const int tid = phase_tid(), lane = tid & 63, wid = phase_wid(tid), fr = lane & 15, fq = lane >> 4;
;     LAS float*  XC  = (LAS float*)lds;
;     LAS bf16_t* XCb = (LAS bf16_t*)(lds + 33792);
;     LAS float*  AA  = (LAS float*)(lds + 51200);
;     LAS float*  SEG = (LAS float*)(lds + 84992);
;     LAS bf16_t* WR  = (LAS bf16_t*)(lds + 89088);
;     LAS bf16_t* WI  = (LAS bf16_t*)(lds + 123904);
;     LAS float*  BB  = XC;
;     const int st = wid & 3, jt0 = (wid >> 2) * 4;
;     const int m = tid >> 3, part = tid & 7, j0 = part * 16;
;     const int sj = tid & 127, seg = tid >> 7;
;     int gcur = -1;
;     float bra[4], bri[4], ls[4]; float cw0[4], cw1[4], cb0 = 0.f, cb1 = 0.f;
;     unsigned xnext[11]; u32x4 gnext[2] = {(u32x4){0u, 0u, 0u, 0u}, (u32x4){0u, 0u, 0u, 0u}}; float hnext = 0.f;
;     auto issue = [&](int unit) {
;         const int n = unit >> 3, c0 = (unit & 7) * 128;
;         const int r0 = n * 64 + wid * 8 - 3;
; #pragma unroll
;         for (int q = 0; q < 11; ++q) { const int row = r0 + q; xnext[q] = row >= 0 ? *(const unsigned*)(proj + (size_t)row * INC + 4096 + c0 + 2 * lane) : 0u; }
;         if (MODE != 0) {
;             const bf16_t* gp = proj + (size_t)(n * 64 + m) * INC + 5120 + c0 + j0;
;             gnext[0] = *(const u32x4*)gp; gnext[1] = *(const u32x4*)(gp + 8);
;             if (MODE == 1) hnext = Hin[n * 1024 + c0 + sj];
;         }
;     };
;     if (b < NCH * 8) issue(b);
.LBB0_238:
	s_add_u32 s4, s92, 0x2000000
	s_addc_u32 s5, s93, 0
	s_add_u32 s86, s92, 0x1d00000
	s_addc_u32 s87, s93, 0
	s_add_u32 s70, s92, 0x1a00000
	s_addc_u32 s71, s93, 0
	s_add_u32 s94, s92, 0x1b00000
	v_writelane_b32 v242, s4, 28
	s_addc_u32 s95, s93, 0
	s_andn2_b64 vcc, exec, s[0:1]
	v_writelane_b32 v242, s5, 29
	s_cbranch_vccnz .LBB0_278
	v_ashrrev_i32_e32 v17, 2, v11
	s_movk_i32 s4, 0x110
	s_lshl_b32 s8, s53, 4
	v_and_b32_e32 v81, 15, v11
	v_lshrrev_b32_e32 v16, 4, v10
	v_and_b32_e32 v80, 0x7f, v11
	v_mul_lo_u32 v20, v17, s4
	s_and_b32 s4, s8, 48
	v_lshlrev_b32_e32 v12, 7, v17
	v_or_b32_e32 v17, s4, v81
	v_lshl_or_b32 v22, v16, 2, s4
	s_add_i32 s4, 0, 0x14c00
	v_lshlrev_b32_e32 v23, 2, v80
	v_mul_u32_u24_e32 v17, 0x110, v17
	v_lshlrev_b32_e32 v21, 3, v16
	v_and_b32_e32 v18, 48, v10
	v_and_b32_e32 v16, 0x3fffff80, v11
	v_add_u32_e32 v112, s4, v23
	s_movk_i32 s9, 0x84
	v_add3_u32 v111, 0, v17, v18
	v_lshl_add_u32 v113, v16, 2, v112
	v_mad_u64_u32 v[16:17], s[4:5], v79, s9, v[78:79]
	v_mbcnt_hi_u32_b32 v17, -1, v202
	v_and_b32_e32 v18, 64, v17
	v_add_u32_e32 v18, 64, v18
	v_xor_b32_e32 v24, 1, v17
	v_cmp_lt_i32_e32 vcc, v24, v18
	v_ashrrev_i32_e32 v19, 7, v11
	v_lshlrev_b32_e32 v11, 6, v11
	v_cndmask_b32_e32 v24, v17, v24, vcc
	v_lshlrev_b32_e32 v114, 2, v24
	v_xor_b32_e32 v24, 2, v17
	v_cmp_lt_i32_e32 vcc, v24, v18
	s_and_b32 s65, s8, 0xffffffc0
	s_movk_i32 s4, 0x88
	v_cndmask_b32_e32 v24, v17, v24, vcc
	v_lshlrev_b32_e32 v115, 2, v24
	v_xor_b32_e32 v24, 4, v17
	v_cmp_lt_i32_e32 vcc, v24, v18
	s_add_i32 s0, 0, 0x15c00
	s_add_i32 s6, 0, 0x1e400
	v_cndmask_b32_e32 v24, v17, v24, vcc
	v_lshlrev_b32_e32 v116, 2, v24
	v_xor_b32_e32 v24, 8, v17
	v_cmp_lt_i32_e32 vcc, v24, v18
	s_or_b32 s63, s8, 48
	v_writelane_b32 v242, s37, 30
	v_cndmask_b32_e32 v24, v17, v24, vcc
	v_lshlrev_b32_e32 v117, 2, v24
	v_xor_b32_e32 v24, 16, v17
	v_cmp_lt_i32_e32 vcc, v24, v18
	v_ashrrev_i32_e32 v13, 31, v12
	v_lshlrev_b64 v[12:13], 1, v[12:13]
	v_cndmask_b32_e32 v24, v17, v24, vcc
	v_lshlrev_b32_e32 v118, 2, v24
	v_xor_b32_e32 v24, 32, v17
	v_cmp_lt_i32_e32 vcc, v24, v18
	v_and_b32_e32 v18, 0xc0, v11
	v_or_b32_e32 v11, s65, v81
	v_cndmask_b32_e32 v17, v17, v24, vcc
	v_lshlrev_b32_e32 v119, 2, v17
	v_mul_lo_u32 v17, v11, s4
	v_add3_u32 v120, s0, v20, v18
	v_add3_u32 v121, s6, v20, v18
	v_add_lshl_u32 v20, v17, v21, 1
	v_add_u32_e32 v122, s0, v20
	v_add_u32_e32 v123, s6, v20
	v_add_u32_e32 v20, 0x880, v17
	v_add_lshl_u32 v24, v20, v21, 1
	v_add_u32_e32 v124, s0, v24
	v_add_u32_e32 v125, s6, v24
	v_add_u32_e32 v24, 0x1100, v17
	v_add_lshl_u32 v25, v24, v21, 1
	v_add_u32_e32 v126, s0, v25
	v_add_u32_e32 v127, s6, v25
	v_or_b32_e32 v25, s63, v81
	v_mul_lo_u32 v26, v25, s4
	v_add_lshl_u32 v27, v26, v21, 1
	v_add_u32_e32 v128, s0, v27
	v_add_u32_e32 v129, s6, v27
	v_or_b32_e32 v27, 32, v21
	v_add_lshl_u32 v28, v17, v27, 1
	v_add_u32_e32 v130, s0, v28
	v_add_u32_e32 v131, s6, v28
	v_add_lshl_u32 v28, v20, v27, 1
	v_add_u32_e32 v132, s0, v28
	v_add_u32_e32 v133, s6, v28
	v_add_lshl_u32 v28, v24, v27, 1
	v_add_lshl_u32 v27, v26, v27, 1
	v_add_u32_e32 v136, s0, v27
	v_add_u32_e32 v137, s6, v27
	v_or_b32_e32 v27, 64, v21
	v_or_b32_e32 v21, 0x60, v21
	v_add_u32_e32 v134, s0, v28
	v_add_u32_e32 v135, s6, v28
	v_add_lshl_u32 v28, v17, v27, 1
	v_add_lshl_u32 v17, v17, v21, 1
	v_add_u32_e32 v146, s0, v17
	v_add_u32_e32 v147, s6, v17
	v_add_lshl_u32 v17, v20, v21, 1
	v_add_u32_e32 v138, s0, v28
	v_add_u32_e32 v139, s6, v28
	v_add_lshl_u32 v28, v20, v27, 1
	v_add_u32_e32 v148, s0, v17
	v_add_u32_e32 v149, s6, v17
	v_add_lshl_u32 v17, v24, v21, 1
	v_add_u32_e32 v140, s0, v28
	v_add_u32_e32 v141, s6, v28
	v_add_lshl_u32 v28, v24, v27, 1
	v_add_lshl_u32 v27, v26, v27, 1
	v_add_u32_e32 v150, s0, v17
	v_add_u32_e32 v151, s6, v17
	v_add_lshl_u32 v17, v26, v21, 1
	v_add_u32_e32 v142, s0, v28
	v_add_u32_e32 v144, s0, v27
	v_add_u32_e32 v152, s0, v17
	s_movk_i32 s0, 0x840
	v_mad_u64_u32 v[20:21], s[4:5], v19, s0, v[80:81]
	s_add_i32 s0, 0, 0x15400
	v_add_u32_e32 v159, s0, v23
	s_add_i32 s0, 0, 0x15600
	v_add_u32_e32 v160, s0, v23
	s_add_i32 s0, 0, 0x14e00
	v_mad_u32_u24 v11, v22, s9, v11
	v_add_u32_e32 v161, s0, v23
	s_add_i32 s0, 0, 0x15800
	v_readlane_b32 s4, v242, 28
	v_mov_b32_e32 v85, 0
	v_lshlrev_b32_e32 v84, 2, v10
	s_lshl_b32 s7, s53, 3
	v_lshl_add_u32 v83, v10, 3, 0
	v_lshl_add_u32 v154, v11, 2, 0
	v_mad_u32_u24 v11, v22, s9, v25
	v_add_u32_e32 v162, s0, v23
	s_add_i32 s0, 0, 0x15000
	v_readlane_b32 s5, v242, 29
	s_mov_b64 s[30:31], s[84:85]
	v_lshl_add_u64 v[14:15], s[44:45], 0, v[12:13]
	v_lshl_add_u64 v[12:13], s[42:43], 0, v[12:13]
	v_lshlrev_b32_e32 v82, 1, v10
	v_sub_u32_e32 v110, v83, v84
	v_cmp_eq_u32_e64 s[38:39], 3, v19
	v_cmp_eq_u32_e64 s[40:41], 0, v10
	s_or_b32 s85, s7, 1
	v_lshl_add_u32 v157, v11, 2, 0
	v_cmp_lt_i32_e64 s[42:43], 0, v19
	v_cmp_lt_i32_e64 s[44:45], 1, v19
	v_cmp_lt_i32_e64 s[46:47], 2, v19
	v_add_u32_e32 v163, s0, v23
	v_lshlrev_b32_e32 v10, 4, v10
	v_mov_b32_e32 v11, v85
	v_lshl_add_u64 v[88:89], s[4:5], 0, v[84:85]
	v_mov_b32_e32 v19, v85
	s_add_i32 s0, s2, s96
	v_mov_b32_e32 v84, v85
	s_mov_b32 s27, s33
	s_mov_b32 s1, 0
	s_mov_b32 s19, -1
	s_mul_i32 s37, s85, 0x210
	s_mulk_i32 s85, 0x110
	v_add_u32_e32 v143, s6, v28
	v_add_u32_e32 v145, s6, v27
	v_add_u32_e32 v153, s6, v17
	v_add_u32_e32 v155, 64, v154
	v_add_u32_e32 v156, 0x80, v154
	v_lshl_add_u32 v158, v20, 2, 0
	v_lshl_add_u32 v164, v16, 2, 0
	v_lshl_add_u64 v[86:87], s[66:67], 0, v[10:11]
	v_lshl_add_u64 v[90:91], v[14:15], 0, v[18:19]
	v_lshl_add_u64 v[92:93], v[12:13], 0, v[18:19]
	s_lshl_b32 s67, s0, 7
	s_lshl_b32 s89, s96, 7
	s_mov_b32 s33, 0xbfb8aa3b
	s_mov_b32 s8, 0x42ce8ed0
	s_mov_b32 s9, 0xc2b17218
	s_mov_b32 s10, 0x7f800000
	s_mov_b32 s11, 0x3f2aaaab
	s_mov_b32 s66, 0x3e9b6dac
	s_mov_b32 s84, 0x3f2aaada
	s_mov_b32 s64, 0x3f317218
	s_mov_b32 s88, 0xb102e308
	s_mov_b32 s12, 0x33800000
	s_mov_b32 s52, 0xc1000000
	s_movk_i32 s13, 0x2000
	s_mov_b32 s14, 0x42fe0000
	s_mov_b32 s15, 0xc0c0400
	s_mov_b32 s16, 0x4000c0c
	v_mov_b32_e32 v165, 0x7f800000
	v_readlane_b32 s17, v243, 8
	s_mov_b32 s21, s2
	v_mov_b64_e32 v[104:105], v[84:85]
	s_waitcnt vmcnt(0)
	s_branch .LBB0_241

; #define LAS __attribute__((address_space(3)))
; template <int MODE> ...
;     ...
;         if (g != gcur) {
;             gcur = g;
;             __syncthreads();
;             {
;                 const int row = tid >> 2, pc = tid & 3;
; #pragma unroll
;                 for (int q = 0; q < 4; ++q) { const int piece = pc * 4 + q;
;                     *(LAS u32x4*)(WR + row * 136 + piece * 8) = *(const u32x4*)(wraT + (size_t)g * 16384 + row * 128 + piece * 8);
;                     *(LAS u32x4*)(WI + row * 136 + piece * 8) = *(const u32x4*)(wriT + (size_t)g * 16384 + row * 128 + piece * 8); }
;             }
; #pragma unroll
;             for (int j = 0; j < 4; ++j) {
;                 const int c = c0 + (jt0 + j) * 16 + fr;
;                 bra[j] = P.b_ra[c]; bri[j] = P.b_ri[c]; ls[j] = -8.0f * log1pf(expf(-P.lam[c]));
;             }
.LBB0_241:
	s_and_b32 s4, s21, 7
	s_lshl_b32 s18, s4, 7
	s_cmp_eq_u32 s4, s19
	s_cbranch_scc1 .LBB0_243
	s_lshl_b32 s0, s4, 15
	v_or_b32_e32 v61, s18, v81
	v_lshl_add_u64 v[34:35], v[90:91], 0, s[0:1]
	v_lshl_add_u64 v[36:37], v[92:93], 0, s[0:1]
	v_add_u32_e32 v38, s65, v61
	s_barrier
	global_load_dwordx4 v[10:13], v[34:35], off offset:32
	global_load_dwordx4 v[14:17], v[34:35], off offset:16
	global_load_dwordx4 v[18:21], v[34:35], off
	global_load_dwordx4 v[22:25], v[36:37], off offset:32
	global_load_dwordx4 v[26:29], v[36:37], off offset:16
	global_load_dwordx4 v[30:33], v[36:37], off
	v_ashrrev_i32_e32 v39, 31, v38
	v_lshlrev_b64 v[46:47], 2, v[38:39]
	v_lshl_add_u64 v[48:49], s[56:57], 0, v[46:47]
	global_load_dword v62, v[48:49], off
	global_load_dword v63, v[48:49], off offset:64
	global_load_dwordx4 v[38:41], v[34:35], off offset:48
	global_load_dwordx4 v[42:45], v[36:37], off offset:48
	v_lshl_add_u64 v[36:37], s[82:83], 0, v[46:47]
	v_lshl_add_u64 v[34:35], s[54:55], 0, v[46:47]
	global_load_dword v46, v[48:49], off offset:128
	s_mov_b32 s0, 0x3ecc95a3
	s_mov_b32 s19, s4
	s_waitcnt vmcnt(8)
	ds_write_b128 v120, v[18:21]
	s_waitcnt vmcnt(5)
	ds_write_b128 v121, v[30:33]
	ds_write_b128 v120, v[14:17] offset:16
	ds_write_b128 v121, v[26:29] offset:16
	ds_write_b128 v120, v[10:13] offset:32
	ds_write_b128 v121, v[22:25] offset:32
	s_waitcnt vmcnt(4)
	v_mul_f32_e32 v10, 0xbfb8aa3b, v62
	s_waitcnt vmcnt(3)
	v_mul_f32_e32 v11, 0xbfb8aa3b, v63
	v_fma_f32 v12, v62, s33, -v10
	v_rndne_f32_e32 v13, v10
	v_fma_f32 v14, v63, s33, -v11
	v_rndne_f32_e32 v15, v11
	v_fmac_f32_e32 v12, 0xb2a5705f, v62
	v_sub_f32_e32 v10, v10, v13
	v_fmac_f32_e32 v14, 0xb2a5705f, v63
	v_sub_f32_e32 v11, v11, v15
	v_add_f32_e32 v10, v10, v12
	v_cvt_i32_f32_e32 v13, v13
	v_add_f32_e32 v11, v11, v14
	v_exp_f32_e32 v10, v10
	v_cvt_i32_f32_e32 v15, v15
	v_exp_f32_e32 v11, v11
	v_cmp_nlt_f32_e32 vcc, s8, v62
	v_ldexp_f32 v10, v10, v13
	s_waitcnt vmcnt(2)
	ds_write_b128 v120, v[38:41] offset:48
	s_waitcnt vmcnt(1)
	ds_write_b128 v121, v[42:45] offset:48
	v_ldexp_f32 v11, v11, v15
	v_cndmask_b32_e32 v10, 0, v10, vcc
	v_cmp_nlt_f32_e32 vcc, s8, v63
	s_nop 1
	v_cndmask_b32_e32 v11, 0, v11, vcc
	v_cmp_ngt_f32_e32 vcc, s9, v62
	s_nop 1
	v_cndmask_b32_e32 v47, v165, v10, vcc
	v_cmp_ngt_f32_e32 vcc, s9, v63
	v_add_f32_e32 v14, 1.0, v47
	v_add_f32_e32 v16, -1.0, v14
	v_cndmask_b32_e32 v48, v165, v11, vcc
	v_add_f32_e32 v15, 1.0, v48
	v_frexp_mant_f32_e32 v19, v15
	v_cvt_f64_f32_e32 v[12:13], v15
	v_frexp_exp_i32_f64_e32 v12, v[12:13]
	v_cmp_gt_f32_e32 vcc, s11, v19
	v_frexp_mant_f32_e32 v17, v14
	v_cvt_f64_f32_e32 v[10:11], v14
	v_add_f32_e32 v18, -1.0, v15
	v_subbrev_co_u32_e32 v30, vcc, 0, v12, vcc
	v_sub_f32_e32 v20, v16, v14
	v_frexp_exp_i32_f64_e32 v10, v[10:11]
	v_sub_f32_e32 v11, v18, v15
	v_cmp_gt_f32_e32 vcc, s11, v17
	v_sub_f32_e32 v16, v47, v16
	v_sub_f32_e32 v18, v48, v18
	v_add_f32_e32 v13, 1.0, v20
	v_add_f32_e32 v11, 1.0, v11
	v_subbrev_co_u32_e32 v31, vcc, 0, v10, vcc
	v_add_f32_e32 v12, v16, v13
	v_add_f32_e32 v13, v18, v11
	v_sub_u32_e32 v11, 0, v31
	v_sub_u32_e32 v16, 0, v30
	v_ldexp_f32 v10, v14, v11
	v_ldexp_f32 v12, v12, v11
	v_ldexp_f32 v11, v15, v16
	v_pk_add_f32 v[14:15], v[10:11], 1.0 op_sel_hi:[1,0]
	v_ldexp_f32 v13, v13, v16
	v_pk_add_f32 v[16:17], v[10:11], -1.0 op_sel_hi:[1,0]
	v_pk_add_f32 v[18:19], v[14:15], -1.0 op_sel_hi:[1,0]
	v_pk_add_f32 v[20:21], v[16:17], 1.0 op_sel_hi:[1,0]
	v_pk_add_f32 v[18:19], v[10:11], v[18:19] neg_lo:[0,1] neg_hi:[0,1]
	v_pk_add_f32 v[10:11], v[10:11], v[20:21] neg_lo:[0,1] neg_hi:[0,1]
	v_pk_add_f32 v[18:19], v[12:13], v[18:19]
	v_pk_add_f32 v[10:11], v[12:13], v[10:11]
	v_pk_add_f32 v[12:13], v[14:15], v[18:19]
	v_pk_add_f32 v[20:21], v[16:17], v[10:11]
	v_rcp_f32_e32 v22, v12
	v_rcp_f32_e32 v23, v13
	v_pk_add_f32 v[16:17], v[16:17], v[20:21] neg_lo:[0,1] neg_hi:[0,1]
	v_pk_add_f32 v[14:15], v[14:15], v[12:13] neg_lo:[0,1] neg_hi:[0,1]
	v_pk_add_f32 v[10:11], v[10:11], v[16:17]
	v_pk_mul_f32 v[16:17], v[20:21], v[22:23]
	v_pk_add_f32 v[14:15], v[18:19], v[14:15]
	v_pk_mul_f32 v[18:19], v[12:13], v[16:17]
	v_cmp_neq_f32_e32 vcc, s10, v47
	v_pk_fma_f32 v[24:25], v[16:17], v[12:13], v[18:19] neg_lo:[0,0,1] neg_hi:[0,0,1]
	s_nop 0
	v_pk_fma_f32 v[24:25], v[16:17], v[14:15], v[24:25]
	s_nop 0
	v_pk_add_f32 v[26:27], v[18:19], v[24:25]
	s_nop 0
	v_pk_add_f32 v[28:29], v[20:21], v[26:27] neg_lo:[0,1] neg_hi:[0,1]
	v_pk_add_f32 v[18:19], v[26:27], v[18:19] neg_lo:[0,1] neg_hi:[0,1]
	v_pk_add_f32 v[20:21], v[20:21], v[28:29] neg_lo:[0,1] neg_hi:[0,1]
	v_pk_add_f32 v[18:19], v[18:19], v[24:25] neg_lo:[0,1] neg_hi:[0,1]
	v_pk_add_f32 v[20:21], v[20:21], v[26:27] neg_lo:[0,1] neg_hi:[0,1]
	s_nop 0
	v_pk_add_f32 v[10:11], v[10:11], v[20:21]
	s_nop 0
	v_pk_add_f32 v[10:11], v[18:19], v[10:11]
	s_nop 0
	v_pk_add_f32 v[18:19], v[28:29], v[10:11]
	s_nop 0
	v_pk_mul_f32 v[20:21], v[22:23], v[18:19]
	v_pk_add_f32 v[24:25], v[28:29], v[18:19] neg_lo:[0,1] neg_hi:[0,1]
	v_pk_mul_f32 v[26:27], v[12:13], v[20:21]
	v_pk_add_f32 v[10:11], v[10:11], v[24:25]
	v_pk_fma_f32 v[12:13], v[20:21], v[12:13], v[26:27] neg_lo:[0,0,1] neg_hi:[0,0,1]
	v_pk_add_f32 v[24:25], v[16:17], v[20:21]
	v_pk_fma_f32 v[12:13], v[20:21], v[14:15], v[12:13]
	s_nop 0
	v_pk_add_f32 v[14:15], v[26:27], v[12:13]
	s_nop 0
	v_pk_add_f32 v[28:29], v[18:19], v[14:15] neg_lo:[0,1] neg_hi:[0,1]
	v_pk_add_f32 v[26:27], v[14:15], v[26:27] neg_lo:[0,1] neg_hi:[0,1]
	v_pk_add_f32 v[18:19], v[18:19], v[28:29] neg_lo:[0,1] neg_hi:[0,1]
	v_pk_add_f32 v[12:13], v[26:27], v[12:13] neg_lo:[0,1] neg_hi:[0,1]
	v_pk_add_f32 v[14:15], v[18:19], v[14:15] neg_lo:[0,1] neg_hi:[0,1]
; template <int MODE> ...
;     ...
;             for (int j = 0; j < 4; ++j) {
;                 const int c = c0 + (jt0 + j) * 16 + fr;
;                 bra[j] = P.b_ra[c]; bri[j] = P.b_ri[c]; ls[j] = -8.0f * log1pf(expf(-P.lam[c]));
;             }
	v_cvt_f32_i32_e32 v19, v30
	v_pk_add_f32 v[10:11], v[10:11], v[14:15]
	v_cvt_f32_i32_e32 v18, v31
	v_pk_add_f32 v[10:11], v[12:13], v[10:11]
	v_pk_add_f32 v[12:13], v[24:25], v[16:17] neg_lo:[0,1] neg_hi:[0,1]
	v_pk_add_f32 v[10:11], v[28:29], v[10:11]
	v_pk_add_f32 v[12:13], v[20:21], v[12:13] neg_lo:[0,1] neg_hi:[0,1]
	v_pk_mul_f32 v[10:11], v[22:23], v[10:11]
	v_mov_b64_e32 v[20:21], s[0:1]
	v_pk_add_f32 v[10:11], v[12:13], v[10:11]
	s_nop 0
	v_pk_add_f32 v[12:13], v[24:25], v[10:11]
	s_nop 0
	v_pk_mul_f32 v[16:17], v[12:13], v[12:13]
	v_pk_add_f32 v[14:15], v[12:13], v[24:25] neg_lo:[0,1] neg_hi:[0,1]
	v_pk_fma_f32 v[22:23], v[16:17], s[66:67], v[20:21] op_sel_hi:[1,0,0]
	v_pk_add_f32 v[10:11], v[10:11], v[14:15] neg_lo:[0,1] neg_hi:[0,1]
	v_ldexp_f32 v14, v12, 1
	v_pk_fma_f32 v[22:23], v[16:17], v[22:23], s[84:85] op_sel_hi:[1,1,0]
	v_ldexp_f32 v15, v13, 1
	v_pk_mul_f32 v[12:13], v[12:13], v[16:17]
	v_pk_mul_f32 v[24:25], v[18:19], s[64:65] op_sel_hi:[1,0]
	v_pk_mul_f32 v[12:13], v[12:13], v[22:23]
	v_pk_fma_f32 v[26:27], v[18:19], s[64:65], v[24:25] op_sel_hi:[1,0,1] neg_lo:[0,0,1] neg_hi:[0,0,1]
	v_pk_add_f32 v[16:17], v[14:15], v[12:13]
	v_mov_b32_e32 v29, v15
	v_pk_add_f32 v[14:15], v[16:17], v[14:15] neg_lo:[0,1] neg_hi:[0,1]
	v_ldexp_f32 v10, v10, 1
	v_pk_fma_f32 v[18:19], v[18:19], s[88:89], v[26:27] op_sel_hi:[1,0,1]
	v_ldexp_f32 v11, v11, 1
	v_mov_b32_e32 v23, v13
	v_pk_add_f32 v[12:13], v[12:13], v[14:15] neg_lo:[0,1] neg_hi:[0,1]
	v_mov_b32_e32 v22, v24
	v_mov_b32_e32 v28, v18
	v_pk_add_f32 v[14:15], v[10:11], v[12:13]
	v_mov_b32_e32 v12, v24
	v_mov_b32_e32 v10, v18
	v_pk_add_f32 v[22:23], v[22:23], v[28:29]
	v_pk_add_f32 v[28:29], v[12:13], v[10:11]
	v_mov_b32_e32 v10, v16
	v_mov_b32_e32 v12, v14
	v_pk_add_f32 v[10:11], v[10:11], v[12:13]
	v_pk_add_f32 v[26:27], v[24:25], v[18:19]
	v_pk_add_f32 v[10:11], v[22:23], v[10:11]
	v_add_u32_e32 v22, s63, v61
	v_ashrrev_i32_e32 v23, 31, v22
	v_lshlrev_b64 v[22:23], 2, v[22:23]
	v_lshl_add_u64 v[40:41], s[56:57], 0, v[22:23]
	global_load_dword v49, v[40:41], off
	v_pk_add_f32 v[12:13], v[16:17], v[14:15]
	v_mov_b32_e32 v30, v26
	v_mov_b32_e32 v31, v25
	v_mov_b32_e32 v32, v12
	v_mov_b32_e32 v33, v19
	v_pk_add_f32 v[40:41], v[26:27], v[12:13]
	v_pk_add_f32 v[38:39], v[30:31], v[32:33]
	v_mov_b32_e32 v42, v12
	v_mov_b32_e32 v43, v41
	v_mov_b32_e32 v44, v16
	v_mov_b32_e32 v45, v27
	v_pk_add_f32 v[30:31], v[38:39], v[30:31] neg_lo:[0,1] neg_hi:[0,1]
	v_pk_add_f32 v[42:43], v[42:43], v[44:45] neg_lo:[0,1] neg_hi:[0,1]
	v_pk_add_f32 v[38:39], v[26:27], v[24:25] neg_lo:[0,1] neg_hi:[0,1]
	v_pk_add_f32 v[32:33], v[32:33], v[30:31] neg_lo:[0,1] neg_hi:[0,1]
	v_mov_b32_e32 v44, v26
	v_mov_b32_e32 v45, v41
	v_mov_b32_e32 v25, v43
	v_mov_b32_e32 v31, v17
	v_pk_add_f32 v[16:17], v[12:13], v[16:17] neg_lo:[0,1] neg_hi:[0,1]
	v_pk_add_f32 v[24:25], v[44:45], v[24:25] neg_lo:[0,1] neg_hi:[0,1]
	v_pk_add_f32 v[38:39], v[18:19], v[38:39] neg_lo:[0,1] neg_hi:[0,1]
	v_pk_add_f32 v[10:11], v[10:11], v[30:31] neg_lo:[0,1] neg_hi:[0,1]
	v_pk_add_f32 v[16:17], v[14:15], v[16:17] neg_lo:[0,1] neg_hi:[0,1]
	v_mov_b32_e32 v19, v27
	v_mov_b32_e32 v15, v13
	v_pk_add_f32 v[10:11], v[28:29], v[10:11] neg_lo:[0,1] neg_hi:[0,1]
	v_pk_add_f32 v[18:19], v[18:19], v[24:25] neg_lo:[0,1] neg_hi:[0,1]
	v_pk_add_f32 v[12:13], v[14:15], v[42:43] neg_lo:[0,1] neg_hi:[0,1]
	v_pk_add_f32 v[24:25], v[32:33], v[10:11]
	v_pk_add_f32 v[14:15], v[12:13], v[18:19]
	v_mov_b32_e32 v13, v11
	v_pk_add_f32 v[10:11], v[38:39], v[12:13]
	v_mov_b32_e32 v19, v33
	v_pk_add_f32 v[10:11], v[10:11], v[18:19] neg_lo:[0,1] neg_hi:[0,1]
	v_mov_b32_e32 v12, v14
	v_mov_b32_e32 v13, v25
	v_pk_add_f32 v[12:13], v[12:13], v[10:11] neg_lo:[0,1] neg_hi:[0,1]
	v_pk_add_f32 v[10:11], v[16:17], v[10:11] neg_lo:[0,1] neg_hi:[0,1]
	v_pk_add_f32 v[12:13], v[18:19], v[12:13] neg_lo:[0,1] neg_hi:[0,1]
	global_load_dword v167, v[36:37], off
	global_load_dword v169, v[36:37], off offset:64
	global_load_dword v171, v[36:37], off offset:128
	v_pk_add_f32 v[10:11], v[10:11], v[12:13]
	v_pk_add_f32 v[12:13], v[24:25], v[14:15]
	global_load_dword v173, v[34:35], off
	global_load_dword v174, v[34:35], off offset:64
	global_load_dword v175, v[34:35], off offset:128
	v_pk_add_f32 v[14:15], v[40:41], v[12:13]
	s_nop 0
	v_pk_add_f32 v[16:17], v[14:15], v[40:41] neg_lo:[0,1] neg_hi:[0,1]
	s_nop 0
	v_pk_add_f32 v[12:13], v[12:13], v[16:17] neg_lo:[0,1] neg_hi:[0,1]
	s_waitcnt vmcnt(6)
; template <int MODE> ...
;     ...
;             for (int j = 0; j < 4; ++j) {
;                 const int c = c0 + (jt0 + j) * 16 + fr;
;                 bra[j] = P.b_ra[c]; bri[j] = P.b_ri[c]; ls[j] = -8.0f * log1pf(expf(-P.lam[c]));
;             }
	v_mul_f32_e32 v16, 0xbfb8aa3b, v49
	v_pk_add_f32 v[10:11], v[10:11], v[12:13]
	v_fma_f32 v17, v49, s33, -v16
	v_pk_add_f32 v[10:11], v[14:15], v[10:11]
	v_rndne_f32_e32 v18, v16
	v_cndmask_b32_e32 v10, v165, v10, vcc
	v_cmp_neq_f32_e32 vcc, s10, v48
	v_fmac_f32_e32 v17, 0xb2a5705f, v49
	v_sub_f32_e32 v16, v16, v18
	v_cndmask_b32_e32 v11, v165, v11, vcc
	v_cmp_lt_f32_e64 vcc, |v48|, s12
	v_add_f32_e32 v16, v16, v17
	v_exp_f32_e32 v16, v16
	v_cndmask_b32_e32 v11, v11, v48, vcc
	v_cmp_lt_f32_e64 vcc, |v47|, s12
	v_cvt_i32_f32_e32 v17, v18
	s_nop 0
	v_cndmask_b32_e32 v10, v10, v47, vcc
	v_pk_mul_f32 v[94:95], v[10:11], s[52:53] op_sel_hi:[1,0]
	v_mul_f32_e32 v10, 0xbfb8aa3b, v46
	v_fma_f32 v11, v46, s33, -v10
	v_rndne_f32_e32 v12, v10
	v_fmac_f32_e32 v11, 0xb2a5705f, v46
	v_sub_f32_e32 v10, v10, v12
	v_add_f32_e32 v10, v10, v11
	v_exp_f32_e32 v10, v10
	v_cvt_i32_f32_e32 v11, v12
	v_cmp_nlt_f32_e32 vcc, s8, v46
	v_ldexp_f32 v10, v10, v11
	s_nop 0
	v_cndmask_b32_e32 v10, 0, v10, vcc
	v_cmp_ngt_f32_e32 vcc, s9, v46
	s_nop 1
	v_cndmask_b32_e32 v38, v165, v10, vcc
	v_add_f32_e32 v12, 1.0, v38
	v_add_f32_e32 v10, -1.0, v12
	v_sub_f32_e32 v11, v10, v12
	v_add_f32_e32 v11, 1.0, v11
	v_sub_f32_e32 v10, v38, v10
	v_add_f32_e32 v13, v10, v11
	v_cvt_f64_f32_e32 v[10:11], v12
	v_frexp_exp_i32_f64_e32 v15, v[10:11]
	v_lshl_add_u64 v[10:11], s[82:83], 0, v[22:23]
	global_load_dword v177, v[10:11], off
	v_lshl_add_u64 v[10:11], s[54:55], 0, v[22:23]
	global_load_dword v176, v[10:11], off
	v_ldexp_f32 v10, v16, v17
	v_cmp_nlt_f32_e32 vcc, s8, v49
	v_frexp_mant_f32_e32 v14, v12
	s_nop 0
	v_cndmask_b32_e32 v10, 0, v10, vcc
	v_cmp_ngt_f32_e32 vcc, s9, v49
	s_nop 1
	v_cndmask_b32_e32 v39, v165, v10, vcc
	v_add_f32_e32 v16, 1.0, v39
	v_add_f32_e32 v10, -1.0, v16
	v_sub_f32_e32 v11, v10, v16
	v_add_f32_e32 v11, 1.0, v11
	v_sub_f32_e32 v10, v39, v10
	v_add_f32_e32 v17, v10, v11
	v_frexp_mant_f32_e32 v18, v16
	v_cvt_f64_f32_e32 v[10:11], v16
	v_frexp_exp_i32_f64_e32 v10, v[10:11]
	v_cmp_gt_f32_e32 vcc, s11, v18
	s_nop 1
	v_subbrev_co_u32_e32 v32, vcc, 0, v10, vcc
	v_cmp_gt_f32_e32 vcc, s11, v14
	s_nop 1
	v_subbrev_co_u32_e32 v33, vcc, 0, v15, vcc
	v_sub_u32_e32 v11, 0, v33
	v_ldexp_f32 v10, v12, v11
	v_ldexp_f32 v12, v13, v11
	v_sub_u32_e32 v13, 0, v32
	v_ldexp_f32 v11, v16, v13
	v_pk_add_f32 v[14:15], v[10:11], 1.0 op_sel_hi:[1,0]
	v_ldexp_f32 v13, v17, v13
	v_pk_add_f32 v[16:17], v[14:15], -1.0 op_sel_hi:[1,0]
	v_pk_add_f32 v[24:25], v[10:11], -1.0 op_sel_hi:[1,0]
	v_pk_add_f32 v[16:17], v[10:11], v[16:17] neg_lo:[0,1] neg_hi:[0,1]
	v_pk_add_f32 v[26:27], v[24:25], 1.0 op_sel_hi:[1,0]
	v_pk_add_f32 v[16:17], v[12:13], v[16:17]
	v_pk_add_f32 v[10:11], v[10:11], v[26:27] neg_lo:[0,1] neg_hi:[0,1]
	v_pk_add_f32 v[18:19], v[14:15], v[16:17]
	v_pk_add_f32 v[10:11], v[12:13], v[10:11]
	v_rcp_f32_e32 v22, v18
	v_rcp_f32_e32 v23, v19
	v_pk_add_f32 v[12:13], v[24:25], v[10:11]
	v_pk_add_f32 v[14:15], v[14:15], v[18:19] neg_lo:[0,1] neg_hi:[0,1]
	v_pk_add_f32 v[24:25], v[24:25], v[12:13] neg_lo:[0,1] neg_hi:[0,1]
	v_pk_add_f32 v[14:15], v[16:17], v[14:15]
	v_pk_mul_f32 v[16:17], v[12:13], v[22:23]
	v_pk_add_f32 v[10:11], v[10:11], v[24:25]
	v_pk_mul_f32 v[24:25], v[18:19], v[16:17]
	s_nop 0
	v_pk_fma_f32 v[26:27], v[16:17], v[18:19], v[24:25] neg_lo:[0,0,1] neg_hi:[0,0,1]
	s_nop 0
	v_pk_fma_f32 v[26:27], v[16:17], v[14:15], v[26:27]
	s_nop 0
	v_pk_add_f32 v[28:29], v[24:25], v[26:27]
	s_nop 0
	v_pk_add_f32 v[30:31], v[12:13], v[28:29] neg_lo:[0,1] neg_hi:[0,1]
	v_pk_add_f32 v[24:25], v[28:29], v[24:25] neg_lo:[0,1] neg_hi:[0,1]
	v_pk_add_f32 v[12:13], v[12:13], v[30:31] neg_lo:[0,1] neg_hi:[0,1]
	s_nop 0
	v_pk_add_f32 v[12:13], v[12:13], v[28:29] neg_lo:[0,1] neg_hi:[0,1]
	s_nop 0
	v_pk_add_f32 v[10:11], v[10:11], v[12:13]
	v_pk_add_f32 v[12:13], v[24:25], v[26:27] neg_lo:[0,1] neg_hi:[0,1]
	s_nop 0
	v_pk_add_f32 v[10:11], v[12:13], v[10:11]
	s_nop 0
	v_pk_add_f32 v[12:13], v[30:31], v[10:11]
	s_nop 0
	v_pk_mul_f32 v[24:25], v[22:23], v[12:13]
	s_nop 0
	v_pk_mul_f32 v[26:27], v[18:19], v[24:25]
	s_nop 0
	v_pk_fma_f32 v[18:19], v[24:25], v[18:19], v[26:27] neg_lo:[0,0,1] neg_hi:[0,0,1]
	s_nop 0
	v_pk_fma_f32 v[14:15], v[24:25], v[14:15], v[18:19]
	v_pk_add_f32 v[18:19], v[30:31], v[12:13] neg_lo:[0,1] neg_hi:[0,1]
	s_nop 0
	v_pk_add_f32 v[10:11], v[10:11], v[18:19]
	v_pk_add_f32 v[18:19], v[26:27], v[14:15]
	s_nop 0
	v_pk_add_f32 v[28:29], v[12:13], v[18:19] neg_lo:[0,1] neg_hi:[0,1]
	v_pk_add_f32 v[26:27], v[18:19], v[26:27] neg_lo:[0,1] neg_hi:[0,1]
	v_pk_add_f32 v[12:13], v[12:13], v[28:29] neg_lo:[0,1] neg_hi:[0,1]
	s_nop 0
	v_pk_add_f32 v[12:13], v[12:13], v[18:19] neg_lo:[0,1] neg_hi:[0,1]
	s_nop 0
	v_pk_add_f32 v[10:11], v[10:11], v[12:13]
	v_pk_add_f32 v[12:13], v[26:27], v[14:15] neg_lo:[0,1] neg_hi:[0,1]
	s_nop 0
	v_pk_add_f32 v[10:11], v[12:13], v[10:11]
	v_pk_add_f32 v[12:13], v[16:17], v[24:25]
	v_pk_add_f32 v[10:11], v[28:29], v[10:11]
	v_pk_add_f32 v[14:15], v[12:13], v[16:17] neg_lo:[0,1] neg_hi:[0,1]
	v_pk_mul_f32 v[10:11], v[22:23], v[10:11]
	v_pk_add_f32 v[14:15], v[24:25], v[14:15] neg_lo:[0,1] neg_hi:[0,1]
	v_cvt_f32_i32_e32 v17, v32
	v_pk_add_f32 v[10:11], v[14:15], v[10:11]
	v_cvt_f32_i32_e32 v16, v33
	v_pk_add_f32 v[14:15], v[12:13], v[10:11]
	v_pk_mul_f32 v[22:23], v[16:17], s[64:65] op_sel_hi:[1,0]
	v_pk_add_f32 v[12:13], v[14:15], v[12:13] neg_lo:[0,1] neg_hi:[0,1]
; template <int MODE> ...
;     ...
;             for (int j = 0; j < 4; ++j) {
;                 const int c = c0 + (jt0 + j) * 16 + fr;
;                 bra[j] = P.b_ra[c]; bri[j] = P.b_ri[c]; ls[j] = -8.0f * log1pf(expf(-P.lam[c]));
;             }
; #pragma unroll
;             for (int kk = 0; kk < 4; ++kk) { cw0[kk] = P.conv_w[kk * 1024 + c0 + 2 * lane]; cw1[kk] = P.conv_w[kk * 1024 + c0 + 2 * lane + 1]; }
;             cb0 = P.conv_b[c0 + 2 * lane]; cb1 = P.conv_b[c0 + 2 * lane + 1];
;         }
;         unsigned xcur[11];
; #pragma unroll
;         for (int q = 0; q < 11; ++q) xcur[q] = xnext[q];
;         const u32x4 gc0 = gnext[0], gc1 = gnext[1]; const float hin0 = hnext;
;         if (unit + G < NCH * 8) issue(unit + G);
	v_pk_mul_f32 v[18:19], v[14:15], v[14:15]
	v_pk_add_f32 v[10:11], v[10:11], v[12:13] neg_lo:[0,1] neg_hi:[0,1]
	v_or_b32_e32 v13, s18, v82
	v_lshlrev_b32_e32 v84, 2, v13
	v_lshl_add_u64 v[26:27], s[76:77], 0, v[84:85]
	v_add_co_u32_e32 v28, vcc, 0x1000, v26
	v_pk_fma_f32 v[20:21], v[18:19], s[66:67], v[20:21] op_sel_hi:[1,0,0]
	s_nop 0
	v_addc_co_u32_e32 v29, vcc, 0, v27, vcc
	v_add_co_u32_e32 v30, vcc, 0x2000, v26
	v_ldexp_f32 v12, v14, 1
	s_nop 0
	v_addc_co_u32_e32 v31, vcc, 0, v27, vcc
	v_add_co_u32_e32 v26, vcc, 0x3000, v26
	v_pk_fma_f32 v[20:21], v[18:19], v[20:21], s[84:85] op_sel_hi:[1,1,0]
	s_nop 0
	v_addc_co_u32_e32 v27, vcc, 0, v27, vcc
	global_load_dwordx2 v[98:99], v[28:29], off
	global_load_dwordx2 v[96:97], v[30:31], off
	global_load_dwordx2 v[100:101], v[26:27], off
	global_load_dwordx2 v[102:103], v84, s[76:77]
	global_load_dwordx2 v[104:105], v84, s[78:79]
	v_ldexp_f32 v13, v15, 1
	v_pk_mul_f32 v[14:15], v[14:15], v[18:19]
	v_pk_fma_f32 v[24:25], v[16:17], s[64:65], v[22:23] op_sel_hi:[1,0,1] neg_lo:[0,0,1] neg_hi:[0,0,1]
	v_pk_mul_f32 v[14:15], v[14:15], v[20:21]
	v_mov_b32_e32 v27, v13
	v_pk_add_f32 v[18:19], v[12:13], v[14:15]
	v_ldexp_f32 v10, v10, 1
	v_pk_add_f32 v[12:13], v[18:19], v[12:13] neg_lo:[0,1] neg_hi:[0,1]
	v_pk_fma_f32 v[16:17], v[16:17], s[88:89], v[24:25] op_sel_hi:[1,0,1]
	v_ldexp_f32 v11, v11, 1
	v_pk_add_f32 v[12:13], v[14:15], v[12:13] neg_lo:[0,1] neg_hi:[0,1]
	v_mov_b32_e32 v20, v22
	v_mov_b32_e32 v21, v15
	v_mov_b32_e32 v26, v16
	v_pk_add_f32 v[14:15], v[10:11], v[12:13]
	v_mov_b32_e32 v12, v22
	v_mov_b32_e32 v10, v16
	v_pk_add_f32 v[20:21], v[20:21], v[26:27]
	v_pk_add_f32 v[26:27], v[12:13], v[10:11]
	v_mov_b32_e32 v10, v18
	v_mov_b32_e32 v12, v14
	v_pk_add_f32 v[24:25], v[22:23], v[16:17]
	v_pk_add_f32 v[10:11], v[10:11], v[12:13]
	v_pk_add_f32 v[12:13], v[18:19], v[14:15]
	v_mov_b32_e32 v28, v24
	v_mov_b32_e32 v29, v23
	v_mov_b32_e32 v30, v12
	v_mov_b32_e32 v31, v17
	v_pk_add_f32 v[10:11], v[20:21], v[10:11]
	v_pk_add_f32 v[20:21], v[24:25], v[12:13]
	v_pk_add_f32 v[32:33], v[28:29], v[30:31]
	v_mov_b32_e32 v34, v12
	v_mov_b32_e32 v35, v21
	v_mov_b32_e32 v36, v18
	v_mov_b32_e32 v37, v25
	v_pk_add_f32 v[28:29], v[32:33], v[28:29] neg_lo:[0,1] neg_hi:[0,1]
	v_pk_add_f32 v[34:35], v[34:35], v[36:37] neg_lo:[0,1] neg_hi:[0,1]
	v_pk_add_f32 v[32:33], v[24:25], v[22:23] neg_lo:[0,1] neg_hi:[0,1]
	v_pk_add_f32 v[30:31], v[30:31], v[28:29] neg_lo:[0,1] neg_hi:[0,1]
	v_mov_b32_e32 v36, v24
	v_mov_b32_e32 v37, v21
	v_mov_b32_e32 v23, v35
	v_mov_b32_e32 v29, v19
	v_pk_add_f32 v[18:19], v[12:13], v[18:19] neg_lo:[0,1] neg_hi:[0,1]
	v_pk_add_f32 v[22:23], v[36:37], v[22:23] neg_lo:[0,1] neg_hi:[0,1]
	v_pk_add_f32 v[32:33], v[16:17], v[32:33] neg_lo:[0,1] neg_hi:[0,1]
	v_pk_add_f32 v[10:11], v[10:11], v[28:29] neg_lo:[0,1] neg_hi:[0,1]
	v_pk_add_f32 v[18:19], v[14:15], v[18:19] neg_lo:[0,1] neg_hi:[0,1]
	v_mov_b32_e32 v17, v25
	v_mov_b32_e32 v15, v13
	v_pk_add_f32 v[10:11], v[26:27], v[10:11] neg_lo:[0,1] neg_hi:[0,1]
	v_pk_add_f32 v[16:17], v[16:17], v[22:23] neg_lo:[0,1] neg_hi:[0,1]
	v_pk_add_f32 v[12:13], v[14:15], v[34:35] neg_lo:[0,1] neg_hi:[0,1]
	v_pk_add_f32 v[22:23], v[30:31], v[10:11]
	v_pk_add_f32 v[14:15], v[12:13], v[16:17]
	v_mov_b32_e32 v13, v11
	v_pk_add_f32 v[10:11], v[32:33], v[12:13]
	v_mov_b32_e32 v17, v31
	v_pk_add_f32 v[10:11], v[10:11], v[16:17] neg_lo:[0,1] neg_hi:[0,1]
	v_mov_b32_e32 v12, v14
	v_mov_b32_e32 v13, v23
	v_pk_add_f32 v[12:13], v[12:13], v[10:11] neg_lo:[0,1] neg_hi:[0,1]
	v_pk_add_f32 v[10:11], v[18:19], v[10:11] neg_lo:[0,1] neg_hi:[0,1]
	v_pk_add_f32 v[12:13], v[16:17], v[12:13] neg_lo:[0,1] neg_hi:[0,1]
	v_cmp_neq_f32_e32 vcc, s10, v38
	v_pk_add_f32 v[10:11], v[10:11], v[12:13]
	v_pk_add_f32 v[12:13], v[22:23], v[14:15]
	s_nop 0
	v_pk_add_f32 v[14:15], v[20:21], v[12:13]
	s_nop 0
	v_pk_add_f32 v[16:17], v[14:15], v[20:21] neg_lo:[0,1] neg_hi:[0,1]
	s_nop 0
	v_pk_add_f32 v[12:13], v[12:13], v[16:17] neg_lo:[0,1] neg_hi:[0,1]
	s_nop 0
	v_pk_add_f32 v[10:11], v[10:11], v[12:13]
	s_nop 0
	v_pk_add_f32 v[10:11], v[14:15], v[10:11]
	s_nop 0
	v_cndmask_b32_e32 v10, v165, v10, vcc
	v_cmp_neq_f32_e32 vcc, s10, v39
	s_nop 1
	v_cndmask_b32_e32 v11, v165, v11, vcc
	v_cmp_lt_f32_e64 vcc, |v39|, s12
	s_nop 1
	v_cndmask_b32_e32 v11, v11, v39, vcc
	v_cmp_lt_f32_e64 vcc, |v38|, s12
	s_nop 1
	v_cndmask_b32_e32 v10, v10, v38, vcc
	v_pk_mul_f32 v[106:107], v[10:11], s[52:53] op_sel_hi:[1,0]
	s_waitcnt vmcnt(0)
.LBB0_243:
	s_add_i32 s20, s21, s96
	s_cmpk_gt_i32 s20, 0x7ff
	s_cselect_b64 s[4:5], -1, 0
	s_waitcnt vmcnt(15)
	v_mov_b64_e32 v[16:17], v[4:5]
	v_mov_b64_e32 v[12:13], v[8:9]
	s_and_b64 vcc, exec, s[4:5]
	v_mov_b64_e32 v[14:15], v[2:3]
	v_mov_b64_e32 v[10:11], v[6:7]
	v_mov_b32_e32 v179, v51
	v_mov_b32_e32 v178, v50
	v_mov_b32_e32 v180, v52
	v_mov_b32_e32 v181, v53
	v_mov_b32_e32 v182, v55
	v_mov_b32_e32 v183, v56
	v_mov_b32_e32 v185, v57
	v_mov_b32_e32 v184, v54
	v_mov_b32_e32 v186, v58
	v_mov_b32_e32 v187, v59
	v_mov_b32_e32 v188, v60
	s_cbranch_vccnz .LBB0_261
	s_and_b32 s6, s20, 0x1ffffff8
	s_add_i32 s6, s6, s53
	s_and_b32 s0, s67, 0x380
	s_lshl_b32 s22, s6, 3
	v_mov_b32_e32 v178, 0
	s_cmp_lt_i32 s22, 3
	v_lshlrev_b32_e32 v84, 1, v82
	v_mov_b32_e32 v179, 0
	s_cbranch_scc0 .LBB0_249
	s_cmp_lt_i32 s22, 2
	s_cbranch_scc0 .LBB0_250
